# PEER: gate coefficients leave U pre-scaled by 2048 (V converts them directly, out-of-range batch skips its MFMA block); U token start loads the next activation row straight into its home registers (no
# baseline (speedup 1.0000x reference)
; #define LAS __attribute__((address_space(3)))
; #define U_RANGE(T, P, RLO, RHI, BLO, BHI) PL_RANGE4(T, P, RLO, RHI, BLO, BHI)
; __device__ __forceinline__ void peer_unit(Frame& F, const Args& a, int layer, int unit, bool last) {
;     ...
;     for (int it = 0; it < 16; ++it) {
;         const v4u se = se_pf;
;         if (it < 15) se_pf = *(const v4u*)(SELW + (tokb + it + 1) * 256 + 4 * lane);
;         const unsigned b0 = se.x >> 12, b1 = se.z >> 12;
;         unsigned pos0 = 0u, pos1 = 0u, base = 0u, pk = 0u;
; #pragma unroll
;         for (unsigned k = 0; k < 4; ++k) {
;             const unsigned long long m0 = __builtin_amdgcn_ballot_w64(b0 == k), m1 = __builtin_amdgcn_ballot_w64(b1 == k);
;             const unsigned below = __builtin_amdgcn_mbcnt_hi((unsigned)(m0 >> 32), __builtin_amdgcn_mbcnt_lo((unsigned)m0, 0u)) + __builtin_amdgcn_mbcnt_hi((unsigned)(m1 >> 32), __builtin_amdgcn_mbcnt_lo((unsigned)m1, 0u));
;             if (b0 == k) pos0 = base + below;
;             if (b1 == k) pos1 = base + below + (b0 == k ? 1u : 0u);
;             base += (unsigned)__builtin_popcountll(m0) + (unsigned)__builtin_popcountll(m1);
;             if (k < 3) pk |= base << (8 * k);
;         }
;     ...
;         pos0 = 2 * lane; pos1 = 2 * lane + 1;
;     ...
;         *(LAS v2u*)(sSort + 2 * pos0) = (v2u){se.x, se.y}; *(LAS v2u*)(sSort + 2 * pos1) = (v2u){se.z, se.w};
;         asm volatile("" ::: "memory");
;         const v2u so0 = *(const LAS v2u*)(sSort + 4 * lane), so1 = *(const LAS v2u*)(sSort + 4 * lane + 2); const v4u so = (v4u){so0.x, so0.y, so1.x, so1.y};
;         asm volatile("" ::: "memory");
;         sIdx[it * 64 + lane] = (so0.x & 0xffffu) | (so1.x << 16);
;         (void)so;
;         { const unsigned g0 = so0.y, g1 = so1.y; sCoef[it * 128 + 2 * lane] = __uint_as_float(g0); sCoef[it * 128 + 2 * lane + 1] = __uint_as_float(g1); }
;         if (lane == it) cnts = pk;
;     }
;     ...
;     for (int ps = DBG_U0; ps < UPASS; ++ps) {
;         int lt = 0, lb, lbh; { U_RANGE(lt, ps, r0, r1, b0_, b1_); lb = b0_; lbh = b1_; (void)r0; (void)r1; }
;         unsigned seL = sIdx[lane];
;         long xlo = 0, xhi = 0; const bool dsel = ((lane >> 2) & 3) == (lane >> 4); const unsigned char* N8 = (const unsigned char*)(F.ws + WS_N8); v4u nnx = *(const v4u*)(N8 + tokb * 1024 + 16 * lane);
;         int ct, cb, crl = 0, crh = 0, cbl = 0;
.LBB0_1726:
	s_waitcnt vmcnt(0)
	v_mov_b64_e32 v[16:17], v[4:5]
	v_mov_b64_e32 v[14:15], v[2:3]
	global_load_dwordx4 v[2:5], v[6:7], off
	v_cmp_gt_u32_e32 vcc, s9, v14
	v_cmp_gt_u32_e64 s[38:39], s9, v16
	v_lshrrev_b32_e32 v13, 12, v14
	v_mbcnt_lo_u32_b32 v19, vcc_lo, 0
	v_mbcnt_lo_u32_b32 v20, s38, 0
	v_mbcnt_hi_u32_b32 v19, vcc_hi, v19
	v_mbcnt_hi_u32_b32 v20, s39, v20
	v_add_u32_e32 v21, v20, v19
	v_lshrrev_b32_e32 v18, 12, v16
	v_cndmask_b32_e32 v21, 0, v21, vcc
	v_addc_co_u32_e64 v19, s[40:41], v20, v19, vcc
	s_bcnt1_i32_b64 s5, vcc
	v_cmp_eq_u32_e32 vcc, 1, v13
	v_cndmask_b32_e64 v19, 0, v19, s[38:39]
	s_bcnt1_i32_b64 s30, s[38:39]
	v_cmp_eq_u32_e64 s[38:39], 1, v18
	v_mbcnt_lo_u32_b32 v20, vcc_lo, 0
	s_add_i32 s5, s30, s5
	v_mbcnt_hi_u32_b32 v20, vcc_hi, v20
	v_mbcnt_lo_u32_b32 v22, s38, 0
	v_mbcnt_hi_u32_b32 v22, s39, v22
	v_add_u32_e32 v20, s5, v20
	v_add_u32_e32 v23, v20, v22
	v_addc_co_u32_e64 v20, s[40:41], v20, v22, vcc
	s_bcnt1_i32_b64 s30, vcc
	v_cndmask_b32_e32 v21, v21, v23, vcc
	v_cndmask_b32_e64 v19, v19, v20, s[38:39]
	s_bcnt1_i32_b64 s38, s[38:39]
	s_add_i32 s30, s5, s30
	v_cmp_eq_u32_e32 vcc, 2, v13
	s_add_i32 s30, s30, s38
	v_cmp_eq_u32_e64 s[38:39], 2, v18
	v_mbcnt_lo_u32_b32 v20, vcc_lo, 0
	v_mbcnt_hi_u32_b32 v20, vcc_hi, v20
	v_mbcnt_lo_u32_b32 v22, s38, 0
	v_mbcnt_hi_u32_b32 v22, s39, v22
	v_add_u32_e32 v20, s30, v20
	v_add_u32_e32 v23, v20, v22
	v_addc_co_u32_e64 v20, s[40:41], v20, v22, vcc
	s_bcnt1_i32_b64 s40, vcc
	s_lshl_b32 s42, s30, 8
	v_cndmask_b32_e32 v21, v21, v23, vcc
	v_cndmask_b32_e64 v19, v19, v20, s[38:39]
	s_bcnt1_i32_b64 s38, s[38:39]
	s_add_i32 s30, s30, s40
	v_cmp_eq_u32_e32 vcc, 3, v13
	s_add_i32 s30, s30, s38
	v_cmp_eq_u32_e64 s[38:39], 3, v18
	v_mbcnt_lo_u32_b32 v13, vcc_lo, 0
	v_mbcnt_hi_u32_b32 v13, vcc_hi, v13
	v_mbcnt_lo_u32_b32 v18, s38, 0
	v_mbcnt_hi_u32_b32 v18, s39, v18
	v_add_u32_e32 v13, s30, v13
	v_add_u32_e32 v20, v13, v18
	v_cndmask_b32_e32 v20, v21, v20, vcc
	v_addc_co_u32_e32 v13, vcc, v13, v18, vcc
	v_cndmask_b32_e64 v13, v19, v13, s[38:39]
	v_lshl_add_u32 v18, v20, 3, s33
	v_lshl_add_u32 v13, v13, 3, s33
	ds_write_b64 v18, v[14:15]
	ds_write_b64 v13, v[16:17]
	ds_read_b128 v[14:17], v10
	s_lshl_b32 s30, s30, 16
	s_or_b32 s30, s42, s30
	s_or_b32 s5, s30, s5
	s_waitcnt lgkmcnt(0)
	v_and_b32_e32 v13, 0xffff, v14
	v_lshl_or_b32 v13, v16, 16, v13
	ds_write_b32 v11, v13
	v_mov_b32_e32 v16, v15
	v_mov_b32_e32 v13, s5
	v_cmp_eq_u32_e32 vcc, s3, v74
	s_add_i32 s3, s3, 1
	s_mov_b64 s[38:39], 0x400
	ds_write_b64 v12, v[16:17]
	v_cndmask_b32_e32 v9, v9, v13, vcc
	v_add_u32_e32 v12, 0x200, v12
	v_add_u32_e32 v11, 0x100, v11
	s_cmp_eq_u32 s3, 15
	v_lshl_add_u64 v[6:7], v[6:7], 0, s[38:39]
	s_cbranch_scc0 .LBB0_1726
	s_waitcnt vmcnt(0)
	v_cmp_gt_u32_e32 vcc, s9, v2
	v_cmp_gt_u32_e64 s[38:39], s9, v4
	s_add_u32 s3, s18, s76
	v_mbcnt_lo_u32_b32 v11, vcc_lo, 0
	v_mbcnt_lo_u32_b32 v12, s38, 0
	s_addc_u32 s5, s19, 0
	v_mbcnt_hi_u32_b32 v11, vcc_hi, v11
	v_mbcnt_hi_u32_b32 v12, s39, v12
	s_add_u32 s42, s3, 0x2800000
	v_lshrrev_b32_e32 v6, 12, v2
	v_add_u32_e32 v13, v12, v11
	s_addc_u32 s43, s5, 0
	v_lshrrev_b32_e32 v7, 12, v4
	v_cndmask_b32_e32 v13, 0, v13, vcc
	v_addc_co_u32_e64 v11, s[40:41], v12, v11, vcc
	s_bcnt1_i32_b64 s5, vcc
	v_cmp_eq_u32_e32 vcc, 1, v6
	v_cndmask_b32_e64 v11, 0, v11, s[38:39]
	s_bcnt1_i32_b64 s30, s[38:39]
	v_cmp_eq_u32_e64 s[38:39], 1, v7
	v_mbcnt_lo_u32_b32 v12, vcc_lo, 0
	s_add_i32 s5, s30, s5
	v_mbcnt_hi_u32_b32 v12, vcc_hi, v12
	v_mbcnt_lo_u32_b32 v14, s38, 0
	v_mbcnt_hi_u32_b32 v14, s39, v14
	v_add_u32_e32 v12, s5, v12
	v_add_u32_e32 v15, v12, v14
	v_addc_co_u32_e64 v12, s[40:41], v12, v14, vcc
	s_bcnt1_i32_b64 s30, vcc
	v_cndmask_b32_e32 v13, v13, v15, vcc
	v_cndmask_b32_e64 v11, v11, v12, s[38:39]
	s_bcnt1_i32_b64 s38, s[38:39]
	s_add_i32 s30, s5, s30
	v_cmp_eq_u32_e32 vcc, 2, v6
	s_add_i32 s30, s30, s38
	v_cmp_eq_u32_e64 s[38:39], 2, v7
	v_mbcnt_lo_u32_b32 v12, vcc_lo, 0
	v_mbcnt_hi_u32_b32 v12, vcc_hi, v12
	v_mbcnt_lo_u32_b32 v14, s38, 0
	v_mbcnt_hi_u32_b32 v14, s39, v14
	v_add_u32_e32 v12, s30, v12
	v_add_u32_e32 v15, v12, v14
	v_addc_co_u32_e64 v12, s[40:41], v12, v14, vcc
	s_bcnt1_i32_b64 s40, vcc
	s_lshl_b32 s44, s30, 8
	v_cndmask_b32_e32 v13, v13, v15, vcc
	v_cndmask_b32_e64 v11, v11, v12, s[38:39]
	s_bcnt1_i32_b64 s38, s[38:39]
	s_add_i32 s30, s30, s40
	v_cmp_eq_u32_e32 vcc, 3, v6
	s_add_i32 s30, s30, s38
	v_cmp_eq_u32_e64 s[38:39], 3, v7
	v_mbcnt_lo_u32_b32 v6, vcc_lo, 0
	v_mbcnt_hi_u32_b32 v6, vcc_hi, v6
	v_mbcnt_lo_u32_b32 v7, s38, 0
	v_mbcnt_hi_u32_b32 v7, s39, v7
	v_add_u32_e32 v6, s30, v6
	v_add_u32_e32 v12, v6, v7
	v_cndmask_b32_e32 v12, v13, v12, vcc
	v_addc_co_u32_e32 v6, vcc, v6, v7, vcc
	v_cndmask_b32_e64 v6, v11, v6, s[38:39]
	v_lshl_add_u32 v7, v12, 3, s33
	ds_write_b64 v7, v[2:3]
	v_lshl_add_u32 v2, v6, 3, s33
	ds_write_b64 v2, v[4:5]
	ds_read_b128 v[2:5], v10
	s_lshl_b32 s30, s30, 16
	s_or_b32 s30, s44, s30
	v_lshl_add_u32 v247, v74, 2, s94
	s_or_b32 s5, s30, s5
	s_waitcnt lgkmcnt(0)
	v_and_b32_e32 v2, 0xffff, v2
	v_lshl_or_b32 v2, v4, 16, v2
	ds_write_b32 v247, v2 offset:3840
	v_mov_b32_e32 v2, s5
	v_cmp_eq_u32_e32 vcc, 15, v74
	v_lshlrev_b32_e32 v224, 4, v74
	v_mov_b32_e32 v4, v3
	v_cndmask_b32_e32 v248, v9, v2, vcc
	v_bfe_u32 v2, v74, 2, 2
	v_ashrrev_i32_e32 v225, 31, v224
	s_add_u32 s46, s18, 0x26400000
	ds_write_b64 v8, v[4:5] offset:7680
	v_cmp_eq_u32_e64 s[38:39], v2, v1
	v_lshl_add_u64 v[2:3], s[42:43], 0, v[224:225]
	s_mov_b64 s[40:41], 0xe00000
	v_and_b32_e32 v4, 2, v74
	s_addc_u32 s47, s19, 0
	s_waitcnt vmcnt(0) lgkmcnt(0)
	v_lshl_add_u64 v[140:141], v[2:3], 0, s[40:41]
	v_cmp_eq_u32_e64 s[40:41], 0, v4
	v_and_b32_e32 v4, 1, v74
	v_ashrrev_i32_e32 v5, 3, v74
	s_add_u32 s6, s46, s6
	v_cmp_eq_u32_e64 s[42:43], 0, v4
	v_lshlrev_b32_e32 v4, 1, v1
	v_and_b32_e32 v5, -4, v5
	s_addc_u32 s7, s47, s7
	s_mov_b32 s3, 0
	v_cmp_eq_u32_e64 s[44:45], 0, v150
	v_and_or_b32 v152, v4, 2, v5
	v_lshl_add_u64 v[142:143], s[6:7], 0, v[224:225]
	v_lshl_add_u64 v[144:145], s[46:47], 0, v[224:225]
	v_mov_b32_e32 v183, 1.0
	v_cndmask_b32_e64 v184, 0, v183, s[38:39]
	v_cndmask_b32_e64 v185, 0, v184, s[40:41]
	v_cndmask_b32_e64 v186, v184, 0, s[40:41]
	v_cndmask_b32_e64 v174, 0, v185, s[42:43]
	v_cndmask_b32_e64 v175, v185, 0, s[42:43]
	v_cndmask_b32_e64 v176, 0, v186, s[42:43]
	v_cndmask_b32_e64 v177, v186, 0, s[42:43]
	v_mov_b32_e32 v178, 0x39800000
	v_mov_b32_e32 v179, 0x3d372713
	v_mov_b32_e32 v180, 0x3fcc422a
	v_mov_b32_e32 v181, 0xbfb8aa3b
	v_mov_b32_e32 v182, 0x42000000
	s_branch .LBB0_1729

.LBB0_1737:
	s_cmp_lg_u32 s48, s56
	s_cbranch_scc1 .LBB0_1741
	s_waitcnt vmcnt(16)
	v_mov_b32_e32 v148, v68
	v_mov_b32_e32 v149, v69
	v_mov_b32_e32 v146, v70
	v_mov_b32_e32 v147, v71
	s_cmp_eq_u32 s58, 15
	s_cbranch_scc1 .LBB0_1741
	s_ashr_i32 s30, s58, 31
	s_add_u32 s46, s0, s58
	s_addc_u32 s47, s1, s30
	s_lshl_b64 s[46:47], s[46:47], 10
	v_lshl_add_u64 v[136:137], v[144:145], 0, s[46:47]
	global_load_dwordx4 v[68:71], v[136:137], off offset:1024

.LBB0_1758:
	s_and_b32 s30, s46, 0xff
	s_add_i32 s30, s30, 15
	s_and_b32 s30, s30, 0x1f0
	s_min_u32 s47, s30, 0x80
	s_bfe_u32 s30, s46, 0x80008
	s_add_i32 s30, s30, 15
	s_and_b32 s30, s30, 0x1f0
	s_min_u32 s56, s30, 0x80
	s_bfe_u32 s30, s46, 0x80010
	s_add_i32 s30, s30, 15
	s_and_b32 s30, s30, 0x1f0
	s_min_u32 s46, s30, 0x80
	s_and_b64 s[70:71], s[6:7], exec
	s_cselect_b32 s30, s56, s46
	s_and_b64 s[70:71], s[52:53], exec
	s_cselect_b32 s30, s47, s30
	s_and_b64 s[70:71], s[54:55], exec
	s_cselect_b32 s30, 0, s30
	s_lshr_b32 s57, s30, 4
	s_min_u32 s57, s57, 7
	s_cmp_lg_u32 s60, s57
	s_cbranch_scc1 .LBB0_1762
	v_mov_b32_e32 v148, v68
	v_mov_b32_e32 v149, v69
	v_mov_b32_e32 v146, v70
	v_mov_b32_e32 v147, v71
	s_cmp_eq_u32 s59, 15
	s_cbranch_scc1 .LBB0_1762
	s_ashr_i32 s57, s59, 31
	s_add_u32 s70, s0, s59
	s_addc_u32 s71, s1, s57
	s_lshl_b64 s[70:71], s[70:71], 10
	v_lshl_add_u64 v[136:137], v[144:145], 0, s[70:71]
	global_load_dwordx4 v[68:71], v[136:137], off offset:1024

.Lpv_skip1:
	s_lshl_b32 s30, s56, 4
	s_cmp_ge_i32 s30, s60
	s_cselect_b64 s[38:39], -1, 0
	s_cmp_lt_i32 s30, s48
	s_cselect_b64 s[52:53], -1, 0
	s_waitcnt lgkmcnt(0)
	s_and_b64 vcc, s[38:39], s[52:53]
	s_cbranch_scc0 .Lpv_h1_out
	v_cvt_pk_fp8_f32 v2, v170, v170
	v_cvt_pk_fp8_f32 v170, v171, v171
	v_mov_b32_e32 v3, v0
	v_perm_b32 v2, v2, v2, v249
	v_mov_b32_e32 v1, v2
	s_nop 0
	v_mfma_f32_16x16x32_fp8_fp8 v[160:163], v[2:3], v[68:69], v[160:163]
	v_mfma_f32_16x16x32_fp8_fp8 v[152:155], v[2:3], v[70:71], v[152:155]
	v_perm_b32 v2, v170, v170, v249
	v_cvt_pk_fp8_f32 v170, v172, v172
	v_mfma_f32_16x16x32_fp8_fp8 v[164:167], v[0:1], v[68:69], v[164:167]
	v_mfma_f32_16x16x32_fp8_fp8 v[156:159], v[0:1], v[70:71], v[156:159]
	v_mov_b32_e32 v1, v2
	v_mfma_f32_16x16x32_fp8_fp8 v[160:163], v[2:3], v[72:73], v[160:163]
	v_mfma_f32_16x16x32_fp8_fp8 v[152:155], v[2:3], v[74:75], v[152:155]
	v_perm_b32 v2, v170, v170, v249
	s_nop 0
	s_nop 0
	v_mfma_f32_16x16x32_fp8_fp8 v[184:187], v[2:3], v[76:77], v[160:163]
	s_nop 1
	s_nop 1
	v_cvt_pk_fp8_f32 v170, v173, v173
	v_mfma_f32_16x16x32_fp8_fp8 v[164:167], v[0:1], v[72:73], v[164:167]
	v_mfma_f32_16x16x32_fp8_fp8 v[156:159], v[0:1], v[74:75], v[156:159]
	v_mov_b32_e32 v1, v2
	v_mfma_f32_16x16x32_fp8_fp8 v[160:163], v[2:3], v[78:79], v[152:155]
	v_perm_b32 v2, v170, v170, v249
	ds_read_b128 v[170:173], v168 offset:16
	v_mfma_f32_16x16x32_fp8_fp8 v[164:167], v[0:1], v[76:77], v[164:167]
	s_waitcnt lgkmcnt(0)
	v_cvt_pk_fp8_f32 v170, v170, v170
	v_mfma_f32_16x16x32_fp8_fp8 v[156:159], v[0:1], v[78:79], v[156:159]
	v_mov_b32_e32 v1, v2
	v_mfma_f32_16x16x32_fp8_fp8 v[152:155], v[2:3], v[80:81], v[184:187]
	v_mfma_f32_16x16x32_fp8_fp8 v[160:163], v[2:3], v[82:83], v[160:163]
	v_perm_b32 v2, v170, v170, v249
	v_cvt_pk_fp8_f32 v170, v171, v171
	v_mfma_f32_16x16x32_fp8_fp8 v[164:167], v[0:1], v[80:81], v[164:167]
	v_mfma_f32_16x16x32_fp8_fp8 v[156:159], v[0:1], v[82:83], v[156:159]
	v_mov_b32_e32 v1, v2
	v_mfma_f32_16x16x32_fp8_fp8 v[152:155], v[2:3], v[84:85], v[152:155]
	v_mfma_f32_16x16x32_fp8_fp8 v[160:163], v[2:3], v[86:87], v[160:163]
	v_perm_b32 v2, v170, v170, v249
	v_cvt_pk_fp8_f32 v170, v172, v172
	v_mfma_f32_16x16x32_fp8_fp8 v[164:167], v[0:1], v[84:85], v[164:167]
	v_mfma_f32_16x16x32_fp8_fp8 v[156:159], v[0:1], v[86:87], v[156:159]
	v_mov_b32_e32 v1, v2
	v_mfma_f32_16x16x32_fp8_fp8 v[152:155], v[2:3], v[88:89], v[152:155]
	v_mfma_f32_16x16x32_fp8_fp8 v[160:163], v[2:3], v[90:91], v[160:163]
	v_perm_b32 v2, v170, v170, v249
	v_cvt_pk_fp8_f32 v170, v173, v173
	v_mfma_f32_16x16x32_fp8_fp8 v[164:167], v[0:1], v[88:89], v[164:167]
	v_mfma_f32_16x16x32_fp8_fp8 v[156:159], v[0:1], v[90:91], v[156:159]
	v_mov_b32_e32 v1, v2
	v_mfma_f32_16x16x32_fp8_fp8 v[152:155], v[2:3], v[92:93], v[152:155]
	v_mfma_f32_16x16x32_fp8_fp8 v[160:163], v[2:3], v[94:95], v[160:163]
	v_perm_b32 v2, v170, v170, v249
	ds_read_b128 v[170:173], v168 offset:32
	s_waitcnt lgkmcnt(0)
	v_cvt_pk_fp8_f32 v170, v170, v170
	v_mfma_f32_16x16x32_fp8_fp8 v[164:167], v[0:1], v[92:93], v[164:167]
	v_mfma_f32_16x16x32_fp8_fp8 v[156:159], v[0:1], v[94:95], v[156:159]
	v_mov_b32_e32 v1, v2
	v_mfma_f32_16x16x32_fp8_fp8 v[152:155], v[2:3], v[96:97], v[152:155]
	v_mfma_f32_16x16x32_fp8_fp8 v[160:163], v[2:3], v[98:99], v[160:163]
	v_perm_b32 v2, v170, v170, v249
	v_cvt_pk_fp8_f32 v170, v171, v171
	v_mfma_f32_16x16x32_fp8_fp8 v[164:167], v[0:1], v[96:97], v[164:167]
	v_mfma_f32_16x16x32_fp8_fp8 v[156:159], v[0:1], v[98:99], v[156:159]
	v_mov_b32_e32 v1, v2
	v_mfma_f32_16x16x32_fp8_fp8 v[152:155], v[2:3], v[100:101], v[152:155]
	v_mfma_f32_16x16x32_fp8_fp8 v[160:163], v[2:3], v[102:103], v[160:163]
	v_perm_b32 v2, v170, v170, v249
	v_cvt_pk_fp8_f32 v170, v172, v172
	v_mfma_f32_16x16x32_fp8_fp8 v[164:167], v[0:1], v[100:101], v[164:167]
	v_mfma_f32_16x16x32_fp8_fp8 v[156:159], v[0:1], v[102:103], v[156:159]
	v_mov_b32_e32 v1, v2
	v_mfma_f32_16x16x32_fp8_fp8 v[152:155], v[2:3], v[104:105], v[152:155]
	v_mfma_f32_16x16x32_fp8_fp8 v[160:163], v[2:3], v[106:107], v[160:163]
	v_perm_b32 v2, v170, v170, v249
	v_cvt_pk_fp8_f32 v170, v173, v173
	v_mfma_f32_16x16x32_fp8_fp8 v[164:167], v[0:1], v[104:105], v[164:167]
	v_mfma_f32_16x16x32_fp8_fp8 v[156:159], v[0:1], v[106:107], v[156:159]
	v_mov_b32_e32 v1, v2
	v_mfma_f32_16x16x32_fp8_fp8 v[152:155], v[2:3], v[108:109], v[152:155]
	v_mfma_f32_16x16x32_fp8_fp8 v[160:163], v[2:3], v[110:111], v[160:163]
	v_perm_b32 v2, v170, v170, v249
	ds_read_b128 v[168:171], v168 offset:48
	v_mfma_f32_16x16x32_fp8_fp8 v[164:167], v[0:1], v[108:109], v[164:167]
	s_waitcnt lgkmcnt(0)
	v_cvt_pk_fp8_f32 v172, v168, v168
	v_mfma_f32_16x16x32_fp8_fp8 v[156:159], v[0:1], v[110:111], v[156:159]
	v_mov_b32_e32 v1, v2
	v_cvt_pk_fp8_f32 v169, v169, v169
	v_mfma_f32_16x16x32_fp8_fp8 v[152:155], v[2:3], v[112:113], v[152:155]
	v_mfma_f32_16x16x32_fp8_fp8 v[160:163], v[2:3], v[114:115], v[160:163]
	v_perm_b32 v2, v172, v172, v249
	v_mfma_f32_16x16x32_fp8_fp8 v[164:167], v[0:1], v[112:113], v[164:167]
	v_mfma_f32_16x16x32_fp8_fp8 v[156:159], v[0:1], v[114:115], v[156:159]
	v_mov_b32_e32 v1, v2
	v_mfma_f32_16x16x32_fp8_fp8 v[152:155], v[2:3], v[120:121], v[152:155]
	s_add_i32 s30, s61, -1
	v_mfma_f32_16x16x32_fp8_fp8 v[160:163], v[2:3], v[122:123], v[160:163]
	v_perm_b32 v2, v169, v169, v249
	v_cvt_pk_fp8_f32 v169, v170, v170
	v_mfma_f32_16x16x32_fp8_fp8 v[164:167], v[0:1], v[120:121], v[164:167]
	s_cmp_lg_u32 s56, s30
	v_mfma_f32_16x16x32_fp8_fp8 v[156:159], v[0:1], v[122:123], v[156:159]
	v_mov_b32_e32 v1, v2
	v_cvt_pk_fp8_f32 v173, v171, v171
	v_mfma_f32_16x16x32_fp8_fp8 v[152:155], v[2:3], v[124:125], v[152:155]
	v_mfma_f32_16x16x32_fp8_fp8 v[160:163], v[2:3], v[126:127], v[160:163]
	v_perm_b32 v2, v169, v169, v249
	v_mfma_f32_16x16x32_fp8_fp8 v[164:167], v[0:1], v[124:125], v[164:167]
	v_mfma_f32_16x16x32_fp8_fp8 v[156:159], v[0:1], v[126:127], v[156:159]
	v_mov_b32_e32 v1, v2
	v_mfma_f32_16x16x32_fp8_fp8 v[152:155], v[2:3], v[144:145], v[152:155]
	v_mfma_f32_16x16x32_fp8_fp8 v[168:171], v[2:3], v[146:147], v[160:163]
	v_perm_b32 v2, v173, v173, v249
	v_mfma_f32_16x16x32_fp8_fp8 v[164:167], v[0:1], v[144:145], v[164:167]
	v_mfma_f32_16x16x32_fp8_fp8 v[156:159], v[0:1], v[146:147], v[156:159]
	v_mov_b32_e32 v1, v2
	s_nop 0
	v_mfma_f32_16x16x32_fp8_fp8 v[160:163], v[2:3], v[148:149], v[152:155]
	v_mfma_f32_16x16x32_fp8_fp8 v[164:167], v[0:1], v[148:149], v[164:167]
	v_mfma_f32_16x16x32_fp8_fp8 v[152:155], v[2:3], v[150:151], v[168:171]
	v_mfma_f32_16x16x32_fp8_fp8 v[156:159], v[0:1], v[150:151], v[156:159]
; __device__ __forceinline__ void peer_token_end(Frame& F, const Args& a, int layer, bool last, bool final_half, size_t tok, int lane, const f32x2 (&out)[8], const f32x4 (&hpre)[4], const v4u (&gpre)[2], const v4u& p8pre) {
;     float* hp = F.h + tok * 1024 + 16 * lane;
;     f32x4 hv[4], ge[4]; float s = 0.f;
;     f32x4 pe[4];
; #pragma unroll
;     for (int i = 0; i < 4; ++i) { const f32x2 lo = __builtin_amdgcn_cvt_pk_f32_fp8((int)p8pre[i], false), hi = __builtin_amdgcn_cvt_pk_f32_fp8((int)p8pre[i], true);
;         pe[i] = (f32x4){lo.x, lo.y, hi.x, hi.y} * (1.f / 256.f) + (f32x4){out[2 * i].x, out[2 * i].y, out[2 * i + 1].x, out[2 * i + 1].y}; }
;     if (!final_half) {
;         v4u w;
; #pragma unroll
;         for (int i = 0; i < 4; ++i) { const f32x4 s8 = pe[i] * 256.f; int t = 0; t = __builtin_amdgcn_cvt_pk_fp8_f32(s8.x, s8.y, t, false); t = __builtin_amdgcn_cvt_pk_fp8_f32(s8.z, s8.w, t, true); w[i] = (unsigned)t; }
;         *(v4u*)((unsigned char*)(F.ws + WS_P8) + tok * 1024 + 16 * lane) = w;
;         return; }
.Lpv_h1_end:
	s_cbranch_scc1 .LBB0_1816
	v_cvt_pk_f32_fp8_e32 v[2:3], v140
	v_cvt_pk_f32_fp8_e32 v[170:171], v141
	v_cvt_pk_f32_fp8_sdwa v[172:173], v141 src0_sel:WORD_1
	v_cvt_pk_f32_fp8_sdwa v[188:189], v142 src0_sel:WORD_1
	v_pk_mul_f32 v[2:3], v[2:3], s[12:13] op_sel_hi:[1,0]
	v_cvt_pk_f32_fp8_e32 v[186:187], v142
	v_pk_fma_f32 v[174:175], v[160:161], s[14:15], v[2:3] op_sel_hi:[1,0,1]
	v_pk_mul_f32 v[2:3], v[170:171], s[12:13] op_sel_hi:[1,0]
	v_pk_mul_f32 v[170:171], v[172:173], s[12:13] op_sel_hi:[1,0]
	v_cvt_pk_f32_fp8_sdwa v[168:169], v140 src0_sel:WORD_1
	v_pk_fma_f32 v[172:173], v[166:167], s[14:15], v[170:171] op_sel_hi:[1,0,1]
	v_pk_mul_f32 v[170:171], v[188:189], s[12:13] op_sel_hi:[1,0]
	v_cvt_pk_f32_fp8_e32 v[188:189], v143
	v_cvt_pk_f32_fp8_sdwa v[192:193], v143 src0_sel:WORD_1
	s_ashr_i32 s30, s58, 31
	s_add_u32 s52, s0, s58
	v_pk_fma_f32 v[184:185], v[164:165], s[14:15], v[2:3] op_sel_hi:[1,0,1]
	v_pk_mul_f32 v[2:3], v[186:187], s[12:13] op_sel_hi:[1,0]
	s_addc_u32 s53, s1, s30
	v_pk_mul_f32 v[168:169], v[168:169], s[12:13] op_sel_hi:[1,0]
	v_pk_fma_f32 v[186:187], v[154:155], s[14:15], v[170:171] op_sel_hi:[1,0,1]
	v_pk_fma_f32 v[190:191], v[152:153], s[14:15], v[2:3] op_sel_hi:[1,0,1]
	v_pk_mul_f32 v[2:3], v[188:189], s[12:13] op_sel_hi:[1,0]
	v_pk_mul_f32 v[170:171], v[192:193], s[12:13] op_sel_hi:[1,0]
	s_lshl_b64 s[38:39], s[52:53], 10
	v_pk_fma_f32 v[168:169], v[162:163], s[14:15], v[168:169] op_sel_hi:[1,0,1]
	v_pk_fma_f32 v[188:189], v[158:159], s[14:15], v[170:171] op_sel_hi:[1,0,1]
	v_pk_fma_f32 v[192:193], v[156:157], s[14:15], v[2:3] op_sel_hi:[1,0,1]
	s_andn2_b64 vcc, exec, s[46:47]
	s_mov_b64 s[54:55], -1
	s_cbranch_vccnz .LBB0_1811
	v_pk_mul_f32 v[2:3], v[174:175], s[8:9] op_sel_hi:[1,0]
	v_mov_b32_e32 v194, v0
	v_cvt_pk_fp8_f32 v194, v2, v3
	v_pk_mul_f32 v[2:3], v[184:185], s[8:9] op_sel_hi:[1,0]
	v_mov_b32_e32 v195, v0
	v_cvt_pk_fp8_f32 v195, v2, v3
	v_pk_mul_f32 v[2:3], v[168:169], s[8:9] op_sel_hi:[1,0]
	v_mov_b32_e32 v196, v0
	v_cvt_pk_fp8_f32 v194, v2, v3 op_sel:[0,0,1]
	v_pk_mul_f32 v[2:3], v[172:173], s[8:9] op_sel_hi:[1,0]
	v_mov_b32_e32 v197, v0
	v_cvt_pk_fp8_f32 v195, v2, v3 op_sel:[0,0,1]
	v_pk_mul_f32 v[2:3], v[190:191], s[8:9] op_sel_hi:[1,0]
	s_mov_b64 s[54:55], 0
	v_cvt_pk_fp8_f32 v196, v2, v3
	v_pk_mul_f32 v[2:3], v[192:193], s[8:9] op_sel_hi:[1,0]
	s_nop 0
	v_cvt_pk_fp8_f32 v197, v2, v3
	v_pk_mul_f32 v[2:3], v[186:187], s[8:9] op_sel_hi:[1,0]
	s_nop 0
	v_cvt_pk_fp8_f32 v196, v2, v3 op_sel:[0,0,1]
	v_pk_mul_f32 v[2:3], v[188:189], s[8:9] op_sel_hi:[1,0]
	s_nop 0
	v_cvt_pk_fp8_f32 v197, v2, v3 op_sel:[0,0,1]
	v_lshl_add_u64 v[2:3], v[234:235], 0, s[38:39]
	global_store_dwordx4 v[2:3], v[194:197], off

.LBB0_1842:
	s_and_b64 s[38:39], s[6:7], exec
	s_cselect_b32 s52, s61, 0x80
	s_and_b64 s[38:39], s[40:41], exec
	s_cselect_b32 s52, s60, s52
	s_and_b64 s[38:39], s[42:43], exec
	s_cselect_b32 s39, s48, s52
	s_lshl_b32 s52, s57, 9
	s_add_i32 s52, s15, s52
	s_lshl_b32 s53, s59, 6
	s_add_i32 s52, s52, s53
	v_mov_b32_e32 v176, s52
	s_lshr_b32 s38, s39, 4
	s_add_i32 s70, s70, 1
	ds_read_b128 v[178:181], v176
	s_max_u32 s38, s38, s70
	s_lshl_b32 s48, s59, 4
	s_cmp_ge_i32 s48, s30
	s_cselect_b64 s[52:53], -1, 0
	s_cmp_lt_i32 s48, s39
	s_cselect_b64 s[54:55], -1, 0
	s_waitcnt lgkmcnt(0)
	s_and_b64 vcc, s[52:53], s[54:55]
	s_cbranch_scc0 .Lpv_h2_out
	v_cvt_pk_fp8_f32 v2, v178, v178
	v_cvt_pk_fp8_f32 v178, v179, v179
	v_perm_b32 v2, v2, v2, v249
	v_mov_b32_e32 v3, v0
	s_nop 1
	v_mfma_f32_16x16x32_fp8_fp8 v[160:163], v[2:3], v[4:5], v[160:163]
	v_mov_b32_e32 v1, v2
	v_mfma_f32_16x16x32_fp8_fp8 v[152:155], v[2:3], v[6:7], v[152:155]
	v_perm_b32 v2, v178, v178, v249
	v_cvt_pk_fp8_f32 v178, v180, v180
	v_mfma_f32_16x16x32_fp8_fp8 v[164:167], v[0:1], v[4:5], v[164:167]
	v_mfma_f32_16x16x32_fp8_fp8 v[156:159], v[0:1], v[6:7], v[156:159]
	v_mov_b32_e32 v1, v2
	v_mfma_f32_16x16x32_fp8_fp8 v[160:163], v[2:3], v[8:9], v[160:163]
	v_mfma_f32_16x16x32_fp8_fp8 v[152:155], v[2:3], v[10:11], v[152:155]
	v_perm_b32 v2, v178, v178, v249
	s_nop 0
	s_nop 0
	v_mfma_f32_16x16x32_fp8_fp8 v[182:185], v[2:3], v[12:13], v[160:163]
	s_nop 1
	s_nop 1
	v_cvt_pk_fp8_f32 v178, v181, v181
	v_mfma_f32_16x16x32_fp8_fp8 v[164:167], v[0:1], v[8:9], v[164:167]
	v_mfma_f32_16x16x32_fp8_fp8 v[156:159], v[0:1], v[10:11], v[156:159]
	v_mov_b32_e32 v1, v2
	v_mfma_f32_16x16x32_fp8_fp8 v[160:163], v[2:3], v[14:15], v[152:155]
	v_perm_b32 v2, v178, v178, v249
	ds_read_b128 v[178:181], v176 offset:16
	v_mfma_f32_16x16x32_fp8_fp8 v[164:167], v[0:1], v[12:13], v[164:167]
	s_waitcnt lgkmcnt(0)
	v_cvt_pk_fp8_f32 v178, v178, v178
	v_mfma_f32_16x16x32_fp8_fp8 v[156:159], v[0:1], v[14:15], v[156:159]
	v_mov_b32_e32 v1, v2
	v_mfma_f32_16x16x32_fp8_fp8 v[152:155], v[2:3], v[16:17], v[182:185]
	v_mfma_f32_16x16x32_fp8_fp8 v[160:163], v[2:3], v[18:19], v[160:163]
	v_perm_b32 v2, v178, v178, v249
	v_cvt_pk_fp8_f32 v178, v179, v179
	v_mfma_f32_16x16x32_fp8_fp8 v[164:167], v[0:1], v[16:17], v[164:167]
	v_mfma_f32_16x16x32_fp8_fp8 v[156:159], v[0:1], v[18:19], v[156:159]
	v_mov_b32_e32 v1, v2
	v_mfma_f32_16x16x32_fp8_fp8 v[152:155], v[2:3], v[20:21], v[152:155]
	v_mfma_f32_16x16x32_fp8_fp8 v[160:163], v[2:3], v[22:23], v[160:163]
	v_perm_b32 v2, v178, v178, v249
	v_cvt_pk_fp8_f32 v178, v180, v180
	v_mfma_f32_16x16x32_fp8_fp8 v[164:167], v[0:1], v[20:21], v[164:167]
	v_mfma_f32_16x16x32_fp8_fp8 v[156:159], v[0:1], v[22:23], v[156:159]
	v_mov_b32_e32 v1, v2
	v_mfma_f32_16x16x32_fp8_fp8 v[152:155], v[2:3], v[24:25], v[152:155]
	v_mfma_f32_16x16x32_fp8_fp8 v[160:163], v[2:3], v[26:27], v[160:163]
	v_perm_b32 v2, v178, v178, v249
	v_cvt_pk_fp8_f32 v178, v181, v181
	v_mfma_f32_16x16x32_fp8_fp8 v[164:167], v[0:1], v[24:25], v[164:167]
	v_mfma_f32_16x16x32_fp8_fp8 v[156:159], v[0:1], v[26:27], v[156:159]
	v_mov_b32_e32 v1, v2
	v_mfma_f32_16x16x32_fp8_fp8 v[152:155], v[2:3], v[28:29], v[152:155]
	v_mfma_f32_16x16x32_fp8_fp8 v[160:163], v[2:3], v[30:31], v[160:163]
	v_perm_b32 v2, v178, v178, v249
	ds_read_b128 v[178:181], v176 offset:32
	s_waitcnt lgkmcnt(0)
	v_cvt_pk_fp8_f32 v178, v178, v178
	v_mfma_f32_16x16x32_fp8_fp8 v[164:167], v[0:1], v[28:29], v[164:167]
	v_mfma_f32_16x16x32_fp8_fp8 v[156:159], v[0:1], v[30:31], v[156:159]
	v_mov_b32_e32 v1, v2
	v_mfma_f32_16x16x32_fp8_fp8 v[152:155], v[2:3], v[32:33], v[152:155]
	v_mfma_f32_16x16x32_fp8_fp8 v[160:163], v[2:3], v[34:35], v[160:163]
	v_perm_b32 v2, v178, v178, v249
	v_cvt_pk_fp8_f32 v178, v179, v179
	v_mfma_f32_16x16x32_fp8_fp8 v[164:167], v[0:1], v[32:33], v[164:167]
	v_mfma_f32_16x16x32_fp8_fp8 v[156:159], v[0:1], v[34:35], v[156:159]
	v_mov_b32_e32 v1, v2
	v_mfma_f32_16x16x32_fp8_fp8 v[152:155], v[2:3], v[36:37], v[152:155]
	v_mfma_f32_16x16x32_fp8_fp8 v[160:163], v[2:3], v[38:39], v[160:163]
	v_perm_b32 v2, v178, v178, v249
	v_cvt_pk_fp8_f32 v178, v180, v180
	v_mfma_f32_16x16x32_fp8_fp8 v[164:167], v[0:1], v[36:37], v[164:167]
	v_mfma_f32_16x16x32_fp8_fp8 v[156:159], v[0:1], v[38:39], v[156:159]
	v_mov_b32_e32 v1, v2
	v_mfma_f32_16x16x32_fp8_fp8 v[152:155], v[2:3], v[40:41], v[152:155]
	v_mfma_f32_16x16x32_fp8_fp8 v[160:163], v[2:3], v[42:43], v[160:163]
	v_perm_b32 v2, v178, v178, v249
	v_cvt_pk_fp8_f32 v178, v181, v181
	v_mfma_f32_16x16x32_fp8_fp8 v[164:167], v[0:1], v[40:41], v[164:167]
	v_mfma_f32_16x16x32_fp8_fp8 v[156:159], v[0:1], v[42:43], v[156:159]
	v_mov_b32_e32 v1, v2
	v_mfma_f32_16x16x32_fp8_fp8 v[152:155], v[2:3], v[44:45], v[152:155]
	v_mfma_f32_16x16x32_fp8_fp8 v[160:163], v[2:3], v[46:47], v[160:163]
	v_perm_b32 v2, v178, v178, v249
	ds_read_b128 v[176:179], v176 offset:48
	v_mfma_f32_16x16x32_fp8_fp8 v[164:167], v[0:1], v[44:45], v[164:167]
	s_waitcnt lgkmcnt(0)
	v_cvt_pk_fp8_f32 v180, v176, v176
	v_mfma_f32_16x16x32_fp8_fp8 v[156:159], v[0:1], v[46:47], v[156:159]
	v_mov_b32_e32 v1, v2
	v_cvt_pk_fp8_f32 v177, v177, v177
	v_mfma_f32_16x16x32_fp8_fp8 v[152:155], v[2:3], v[48:49], v[152:155]
	v_mfma_f32_16x16x32_fp8_fp8 v[160:163], v[2:3], v[50:51], v[160:163]
	v_perm_b32 v2, v180, v180, v249
	v_mfma_f32_16x16x32_fp8_fp8 v[164:167], v[0:1], v[48:49], v[164:167]
	v_mfma_f32_16x16x32_fp8_fp8 v[156:159], v[0:1], v[50:51], v[156:159]
	v_mov_b32_e32 v1, v2
	v_mfma_f32_16x16x32_fp8_fp8 v[152:155], v[2:3], v[52:53], v[152:155]
	s_add_i32 s38, s38, -1
	v_mfma_f32_16x16x32_fp8_fp8 v[160:163], v[2:3], v[54:55], v[160:163]
	v_perm_b32 v2, v177, v177, v249
	v_cvt_pk_fp8_f32 v177, v178, v178
	v_mfma_f32_16x16x32_fp8_fp8 v[164:167], v[0:1], v[52:53], v[164:167]
	s_cmp_lg_u32 s59, s38
	v_mfma_f32_16x16x32_fp8_fp8 v[156:159], v[0:1], v[54:55], v[156:159]
	v_mov_b32_e32 v1, v2
	v_cvt_pk_fp8_f32 v181, v179, v179
	v_mfma_f32_16x16x32_fp8_fp8 v[152:155], v[2:3], v[56:57], v[152:155]
	v_mfma_f32_16x16x32_fp8_fp8 v[160:163], v[2:3], v[58:59], v[160:163]
	v_perm_b32 v2, v177, v177, v249
	v_mfma_f32_16x16x32_fp8_fp8 v[164:167], v[0:1], v[56:57], v[164:167]
	v_mfma_f32_16x16x32_fp8_fp8 v[156:159], v[0:1], v[58:59], v[156:159]
	v_mov_b32_e32 v1, v2
	v_mfma_f32_16x16x32_fp8_fp8 v[152:155], v[2:3], v[60:61], v[152:155]
	v_mfma_f32_16x16x32_fp8_fp8 v[176:179], v[2:3], v[62:63], v[160:163]
	v_perm_b32 v2, v181, v181, v249
	v_mfma_f32_16x16x32_fp8_fp8 v[164:167], v[0:1], v[60:61], v[164:167]
	v_mfma_f32_16x16x32_fp8_fp8 v[156:159], v[0:1], v[62:63], v[156:159]
	v_mov_b32_e32 v1, v2
	v_mfma_f32_16x16x32_fp8_fp8 v[160:163], v[2:3], v[64:65], v[152:155]
	s_nop 0
	v_mfma_f32_16x16x32_fp8_fp8 v[164:167], v[0:1], v[64:65], v[164:167]
	v_mfma_f32_16x16x32_fp8_fp8 v[152:155], v[2:3], v[66:67], v[176:179]
	v_mfma_f32_16x16x32_fp8_fp8 v[156:159], v[0:1], v[66:67], v[156:159]
; __device__ __forceinline__ void peer_token_end(Frame& F, const Args& a, int layer, bool last, bool final_half, size_t tok, int lane, const f32x2 (&out)[8], const f32x4 (&hpre)[4], const v4u (&gpre)[2], const v4u& p8pre) {
;     float* hp = F.h + tok * 1024 + 16 * lane;
;     f32x4 hv[4], ge[4]; float s = 0.f;
;     f32x4 pe[4];
; #pragma unroll
;     for (int i = 0; i < 4; ++i) { const f32x2 lo = __builtin_amdgcn_cvt_pk_f32_fp8((int)p8pre[i], false), hi = __builtin_amdgcn_cvt_pk_f32_fp8((int)p8pre[i], true);
;         pe[i] = (f32x4){lo.x, lo.y, hi.x, hi.y} * (1.f / 256.f) + (f32x4){out[2 * i].x, out[2 * i].y, out[2 * i + 1].x, out[2 * i + 1].y}; }
;     if (!final_half) {
;         v4u w;
; #pragma unroll
;         for (int i = 0; i < 4; ++i) { const f32x4 s8 = pe[i] * 256.f; int t = 0; t = __builtin_amdgcn_cvt_pk_fp8_f32(s8.x, s8.y, t, false); t = __builtin_amdgcn_cvt_pk_fp8_f32(s8.z, s8.w, t, true); w[i] = (unsigned)t; }
;         *(v4u*)((unsigned char*)(F.ws + WS_P8) + tok * 1024 + 16 * lane) = w;
;         return; }
.Lpv_h2_end:
	s_cbranch_scc1 .LBB0_1850
	s_waitcnt vmcnt(0)
	v_cvt_pk_f32_fp8_e32 v[2:3], v140
	v_cvt_pk_f32_fp8_e32 v[178:179], v141
	v_cvt_pk_f32_fp8_sdwa v[180:181], v141 src0_sel:WORD_1
	v_cvt_pk_f32_fp8_sdwa v[188:189], v142 src0_sel:WORD_1
	v_pk_mul_f32 v[2:3], v[2:3], s[12:13] op_sel_hi:[1,0]
	v_cvt_pk_f32_fp8_e32 v[186:187], v142
	v_pk_fma_f32 v[182:183], v[160:161], s[14:15], v[2:3] op_sel_hi:[1,0,1]
	v_pk_mul_f32 v[2:3], v[178:179], s[12:13] op_sel_hi:[1,0]
	v_pk_mul_f32 v[178:179], v[180:181], s[12:13] op_sel_hi:[1,0]
	v_cvt_pk_f32_fp8_sdwa v[176:177], v140 src0_sel:WORD_1
	v_pk_fma_f32 v[180:181], v[166:167], s[14:15], v[178:179] op_sel_hi:[1,0,1]
	v_pk_mul_f32 v[178:179], v[188:189], s[12:13] op_sel_hi:[1,0]
	v_cvt_pk_f32_fp8_e32 v[188:189], v143
	v_cvt_pk_f32_fp8_sdwa v[192:193], v143 src0_sel:WORD_1
	s_ashr_i32 s30, s57, 31
	s_add_u32 s52, s0, s57
	v_pk_fma_f32 v[184:185], v[164:165], s[14:15], v[2:3] op_sel_hi:[1,0,1]
	v_pk_mul_f32 v[2:3], v[186:187], s[12:13] op_sel_hi:[1,0]
	s_addc_u32 s53, s1, s30
	v_pk_mul_f32 v[176:177], v[176:177], s[12:13] op_sel_hi:[1,0]
	v_pk_fma_f32 v[186:187], v[154:155], s[14:15], v[178:179] op_sel_hi:[1,0,1]
	v_pk_fma_f32 v[190:191], v[152:153], s[14:15], v[2:3] op_sel_hi:[1,0,1]
	v_pk_mul_f32 v[2:3], v[188:189], s[12:13] op_sel_hi:[1,0]
	v_pk_mul_f32 v[178:179], v[192:193], s[12:13] op_sel_hi:[1,0]
	s_lshl_b64 s[38:39], s[52:53], 10
	v_pk_fma_f32 v[176:177], v[162:163], s[14:15], v[176:177] op_sel_hi:[1,0,1]
	v_pk_fma_f32 v[188:189], v[158:159], s[14:15], v[178:179] op_sel_hi:[1,0,1]
	v_pk_fma_f32 v[192:193], v[156:157], s[14:15], v[2:3] op_sel_hi:[1,0,1]
	s_andn2_b64 vcc, exec, s[46:47]
	s_mov_b64 s[54:55], -1
	s_cbranch_vccnz .LBB0_1845
	v_pk_mul_f32 v[2:3], v[182:183], s[8:9] op_sel_hi:[1,0]
	v_mov_b32_e32 v194, v0
	v_cvt_pk_fp8_f32 v194, v2, v3
	v_pk_mul_f32 v[2:3], v[184:185], s[8:9] op_sel_hi:[1,0]
	v_mov_b32_e32 v195, v0
	v_cvt_pk_fp8_f32 v195, v2, v3
	v_pk_mul_f32 v[2:3], v[176:177], s[8:9] op_sel_hi:[1,0]
	v_mov_b32_e32 v196, v0
	v_cvt_pk_fp8_f32 v194, v2, v3 op_sel:[0,0,1]
	v_pk_mul_f32 v[2:3], v[180:181], s[8:9] op_sel_hi:[1,0]
	v_mov_b32_e32 v197, v0
	v_cvt_pk_fp8_f32 v195, v2, v3 op_sel:[0,0,1]
	v_pk_mul_f32 v[2:3], v[190:191], s[8:9] op_sel_hi:[1,0]
	s_mov_b64 s[54:55], 0
	v_cvt_pk_fp8_f32 v196, v2, v3
	v_pk_mul_f32 v[2:3], v[192:193], s[8:9] op_sel_hi:[1,0]
	s_nop 0
	v_cvt_pk_fp8_f32 v197, v2, v3
	v_pk_mul_f32 v[2:3], v[186:187], s[8:9] op_sel_hi:[1,0]
	s_nop 0
	v_cvt_pk_fp8_f32 v196, v2, v3 op_sel:[0,0,1]
	v_pk_mul_f32 v[2:3], v[188:189], s[8:9] op_sel_hi:[1,0]
	s_nop 0
	v_cvt_pk_fp8_f32 v197, v2, v3 op_sel:[0,0,1]
	v_lshl_add_u64 v[2:3], v[234:235], 0, s[38:39]
	global_store_dwordx4 v[2:3], v[194:197], off

.Lpv_h1_out:
	s_add_i32 s30, s61, -1
	s_cmp_lg_u32 s56, s30
	s_branch .Lpv_h1_end
.Lpv_h2_out:
	s_add_i32 s38, s38, -1
	s_cmp_lg_u32 s59, s38
	s_branch .Lpv_h2_end
